# v93: v92 + M3 pooling loop: redundant end-of-item barrier removed (U rewrite is covered by the item's second barrier, DF rewrite by the next item's first)
# baseline (speedup 1.0000x reference)
.LBB0_578:
	s_andn2_b64 vcc, exec, s[22:23]
	s_add_i32 s2, s2, s80
	s_cbranch_vccz .LBB0_544
